# baseline (speedup 1.0000x reference)
.LBB10_15:
	v_exp_f32_e32 v32, v32
	v_exp_f32_e32 v69, v33
	v_exp_f32_e32 v33, v34
	v_exp_f32_e32 v70, v35
	v_exp_f32_e32 v34, v36
	v_exp_f32_e32 v35, v38
	v_exp_f32_e32 v38, v39
	v_exp_f32_e32 v37, v37
	v_cvt_pk_f16_f32 v33, v33, v70
	v_cvt_pk_f16_f32 v32, v32, v69
	v_cvt_pk_f16_f32 v35, v35, v38
	v_cvt_pk_f16_f32 v34, v34, v37
	v_exp_f32_e32 v40, v40
	v_exp_f32_e32 v42, v42
	s_waitcnt lgkmcnt(1)
	v_mfma_f32_32x32x16_f16 v[0:15], v[56:59], v[32:35], v[0:15]
	v_exp_f32_e32 v36, v44
	v_exp_f32_e32 v39, v46
	v_exp_f32_e32 v44, v47
	v_exp_f32_e32 v32, v45
	v_exp_f32_e32 v33, v43
	v_exp_f32_e32 v37, v41
	v_cvt_pk_f16_f32 v35, v39, v44
	v_cvt_pk_f16_f32 v34, v36, v32
	v_cvt_pk_f16_f32 v33, v42, v33
	v_cvt_pk_f16_f32 v32, v40, v37
	s_add_i32 s3, s3, -1
	s_add_i32 s11, s11, 32
	s_waitcnt lgkmcnt(0)
	v_mfma_f32_32x32x16_f16 v[0:15], v[52:55], v[32:35], v[0:15]
	s_cmp_eq_u32 s3, 0
	s_cbranch_scc1 .LBB10_21

.LBB10_18:
	v_add_u32_e32 v66, 0x400, v66
	s_nop 9
	v_max3_f32 v69, v32, v33, v34
	v_max_f32_e32 v69, v69, v35
	v_max3_f32 v69, v69, v36, v37
	v_max3_f32 v69, v69, v38, v39
	v_max3_f32 v69, v69, v40, v41
	v_max3_f32 v69, v69, v42, v43
	v_max3_f32 v69, v69, v44, v45
	v_max3_f32 v69, v69, v46, v47
	v_cmp_lt_f32_e32 vcc, s15, v69
	s_cbranch_vccz .LBB10_15
	ds_bpermute_b32 v16, v63, v69
	v_mov_b32_e32 v18, v33
	v_mov_b32_e32 v19, v34
	v_mov_b32_e32 v20, v35
	v_mov_b32_e32 v21, v36
	s_waitcnt lgkmcnt(0)
	v_max3_f32 v30, v69, v16, 0
	v_exp_f32_e64 v16, -v30
	v_mov_b32_e32 v22, v37
	v_mov_b32_e32 v23, v38
	v_mov_b32_e32 v24, v39
	v_mov_b32_e32 v25, v40
	v_mov_b32_e32 v26, v41
	v_mov_b32_e32 v27, v42
	v_mov_b32_e32 v28, v43
	v_mov_b32_e32 v29, v44
	v_mov_b32_e32 v34, v45
	v_mov_b32_e32 v35, v46
	v_add_f32_e32 v64, v64, v30
	v_pk_mul_f32 v[0:1], v[16:17], v[0:1] op_sel_hi:[0,1]
	v_pk_mul_f32 v[2:3], v[16:17], v[2:3] op_sel_hi:[0,1]
	v_pk_mul_f32 v[4:5], v[16:17], v[4:5] op_sel_hi:[0,1]
	v_pk_mul_f32 v[6:7], v[16:17], v[6:7] op_sel_hi:[0,1]
	v_mul_f32_e32 v8, v16, v8
	v_xor_b32_e32 v16, 0x80000000, v64
	v_pk_add_f32 v[36:37], v[18:19], v[30:31] op_sel_hi:[1,0] neg_lo:[0,1] neg_hi:[0,1]
	v_pk_add_f32 v[38:39], v[20:21], v[30:31] op_sel_hi:[1,0] neg_lo:[0,1] neg_hi:[0,1]
	v_pk_add_f32 v[40:41], v[22:23], v[30:31] op_sel_hi:[1,0] neg_lo:[0,1] neg_hi:[0,1]
	v_pk_add_f32 v[42:43], v[24:25], v[30:31] op_sel_hi:[1,0] neg_lo:[0,1] neg_hi:[0,1]
	v_pk_add_f32 v[44:45], v[26:27], v[30:31] op_sel_hi:[1,0] neg_lo:[0,1] neg_hi:[0,1]
	v_pk_add_f32 v[70:71], v[28:29], v[30:31] op_sel_hi:[1,0] neg_lo:[0,1] neg_hi:[0,1]
	v_pk_add_f32 v[72:73], v[34:35], v[30:31] op_sel_hi:[1,0] neg_lo:[0,1] neg_hi:[0,1]
	v_sub_f32_e32 v32, v32, v30
	v_sub_f32_e32 v47, v47, v30
	v_mov_b32_e32 v17, v16
	v_mov_b32_e32 v18, v16
	v_mov_b32_e32 v19, v16
	v_mov_b32_e32 v20, v16
	v_mov_b32_e32 v21, v16
	v_mov_b32_e32 v22, v16
	v_mov_b32_e32 v23, v16
	v_mov_b32_e32 v24, v16
	v_mov_b32_e32 v25, v16
	v_mov_b32_e32 v26, v16
	v_mov_b32_e32 v27, v16
	v_mov_b32_e32 v28, v16
	v_mov_b32_e32 v29, v16
	v_mov_b32_e32 v30, v16
	v_mov_b32_e32 v31, v16
	v_mov_b32_e32 v33, v36
	v_mov_b32_e32 v34, v37
	v_mov_b32_e32 v35, v38
	v_mov_b32_e32 v36, v39
	v_mov_b32_e32 v37, v40
	v_mov_b32_e32 v38, v41
	v_mov_b32_e32 v39, v42
	v_mov_b32_e32 v40, v43
	v_mov_b32_e32 v41, v44
	v_mov_b32_e32 v42, v45
	v_mov_b32_e32 v43, v70
	v_mov_b32_e32 v44, v71
	v_mov_b32_e32 v45, v72
	v_mov_b32_e32 v46, v73
	s_branch .LBB10_15
